# merge GEMM epilogues: gate/T1 row loads issued ahead with counted vmcnt (was one round trip per store); MoE down leftover split-K tiles: 6 K-steps of fragment loads in flight
# speedup vs baseline: 1.0005x; 1.0005x over previous
; __device__ __forceinline__ unsigned pk2(float lo, float hi) { f32x2 v = {lo, hi}; return __builtin_bit_cast(unsigned, __builtin_convertvector(v, bf2_t)); }
; template <int BIT = 0> __device__ __forceinline__ void st16w(void* p, u32x4 v) { if ((WT_STORES >> BIT) & 1) asm volatile("global_store_dwordx4 %0, %1, off sc1\n\ts_nop 1" :: "v"(p), "v"(v) : "memory"); else *(u32x4*)p = v; }
; __device__ __forceinline__ float bflo(unsigned u) { return __uint_as_float(u << 16); }
; __device__ __forceinline__ float bfhi(unsigned u) { return __uint_as_float(u & 0xffff0000u); }
;     __device__ __forceinline__ void operator()(const f32x4 (&acc)[2][2][4][2], const Unit& u, int wr, int wc, int fr, int fq) const {
;         const int row0 = u.pm * BM + wr * 64 + fr, col0 = u.pn * BM + wc * 32 + 8 * fq;
; #pragma unroll
;         for (int ai = 0; ai < 2; ++ai)
; #pragma unroll
;             for (int m = 0; m < 4; ++m) {
;                 const size_t row = (size_t)(row0 + ai * HALF + m * 16);
; #pragma unroll
;                 for (int bj = 0; bj < 2; ++bj) {
;                     const int col = col0 + bj * HALF;
;                     const u32x4 g = *(const u32x4*)(P + row * INC + goff + col);
;                     const f32x4 a0 = acc[ai][bj][m][0], a1 = acc[ai][bj][m][1];
;                     float o[8] = {bflo(g.x) * a0[0], bfhi(g.x) * a0[1], bflo(g.y) * a0[2], bfhi(g.y) * a0[3], bflo(g.z) * a1[0], bfhi(g.z) * a1[1], bflo(g.w) * a1[2], bfhi(g.w) * a1[3]};
;                     if (mode) { const u32x4 t = *(const u32x4*)(T1 + row * D + col);
;                         o[0] += bflo(t.x); o[1] += bfhi(t.x); o[2] += bflo(t.y); o[3] += bfhi(t.y); o[4] += bflo(t.z); o[5] += bfhi(t.z); o[6] += bflo(t.w); o[7] += bfhi(t.w); }
;                     u32x4 w; w.x = pk2(o[0], o[1]); w.y = pk2(o[2], o[3]); w.z = pk2(o[4], o[5]); w.w = pk2(o[6], o[7]);
;                     if (mode) st16w(MM + row * D + col, w); else *(u32x4*)(T1 + row * D + col) = w;
.LBB13_825:
	v_readfirstlane_b32 s98, v132
	v_readfirstlane_b32 s99, v133
	v_readfirstlane_b32 s24, v134
	v_readfirstlane_b32 s25, v135
	v_lshl_add_u32 v158, s22, 8, v99
	v_lshl_or_b32 v159, s23, 8, v153
	s_mov_b64 s[22:23], -1
	s_andn2_b64 vcc, exec, s[4:5]
	s_mov_b32 s87, 0x8000
	s_movk_i32 s86, 0x1c00
	v_mul_u32_u24_e32 v156, 0x2c00, v158
	v_lshl_add_u32 v156, v159, 1, v156
	v_add_u32_e32 v156, 0x2400, v156
	v_lshlrev_b32_e32 v157, 11, v158
	v_lshl_add_u32 v157, v159, 1, v157
	global_load_dwordx4 v[160:163], v156, s[98:99]
	global_load_dwordx4 v[164:167], v156, s[98:99] offset:256
	v_add_u32_e32 v158, 0x2c000, v156
	global_load_dwordx4 v[168:171], v158, s[98:99]
	v_add_u32_e32 v158, 0x2c000, v156
	global_load_dwordx4 v[172:175], v158, s[98:99] offset:256
	v_add_u32_e32 v158, 0x58000, v156
	global_load_dwordx4 v[176:179], v158, s[98:99]
	v_add_u32_e32 v158, 0x58000, v156
	global_load_dwordx4 v[180:183], v158, s[98:99] offset:256
	v_add_u32_e32 v158, 0x84000, v156
	global_load_dwordx4 v[184:187], v158, s[98:99]
	v_add_u32_e32 v158, 0x84000, v156
	global_load_dwordx4 v[188:191], v158, s[98:99] offset:256
	v_add_u32_e32 v158, 0x160000, v156
	global_load_dwordx4 v[192:195], v158, s[98:99]
	v_add_u32_e32 v158, 0x160000, v156
	global_load_dwordx4 v[196:199], v158, s[98:99] offset:256
	v_add_u32_e32 v158, 0x18c000, v156
	global_load_dwordx4 v[208:211], v158, s[98:99]
	v_add_u32_e32 v158, 0x18c000, v156
	global_load_dwordx4 v[212:215], v158, s[98:99] offset:256
	v_add_u32_e32 v158, 0x1b8000, v156
	global_load_dwordx4 v[216:219], v158, s[98:99]
	v_add_u32_e32 v158, 0x1b8000, v156
	global_load_dwordx4 v[220:223], v158, s[98:99] offset:256
	s_waitcnt vmcnt(13)
	v_lshlrev_b32_e32 v148, 16, v160
	v_and_b32_e32 v149, 0xffff0000, v160
	v_pk_mul_f32 v[128:129], v[128:129], v[148:149]
	v_lshlrev_b32_e32 v150, 16, v161
	v_and_b32_e32 v151, 0xffff0000, v161
	v_pk_mul_f32 v[130:131], v[130:131], v[150:151]
	v_lshlrev_b32_e32 v148, 16, v162
	v_and_b32_e32 v149, 0xffff0000, v162
	v_pk_mul_f32 v[124:125], v[124:125], v[148:149]
	v_lshlrev_b32_e32 v150, 16, v163
	v_and_b32_e32 v151, 0xffff0000, v163
	v_pk_mul_f32 v[126:127], v[126:127], v[150:151]
	v_cvt_pk_bf16_f32 v128, v128, v129
	v_cvt_pk_bf16_f32 v129, v130, v131
	v_cvt_pk_bf16_f32 v130, v124, v125
	v_cvt_pk_bf16_f32 v131, v126, v127
	global_store_dwordx4 v157, v[128:131], s[24:25]
	v_add_u32_e32 v158, 0x1e4000, v156
	global_load_dwordx4 v[160:163], v158, s[98:99]
	v_add_u32_e32 v158, 0x1e4000, v156
	global_load_dwordx4 v[124:127], v158, s[98:99] offset:256
	s_waitcnt vmcnt(15)
	v_lshlrev_b32_e32 v148, 16, v164
	v_and_b32_e32 v149, 0xffff0000, v164
	v_pk_mul_f32 v[120:121], v[120:121], v[148:149]
	v_lshlrev_b32_e32 v150, 16, v165
	v_and_b32_e32 v151, 0xffff0000, v165
	v_pk_mul_f32 v[122:123], v[122:123], v[150:151]
	v_lshlrev_b32_e32 v148, 16, v166
	v_and_b32_e32 v149, 0xffff0000, v166
	v_pk_mul_f32 v[116:117], v[116:117], v[148:149]
	v_lshlrev_b32_e32 v150, 16, v167
	v_and_b32_e32 v151, 0xffff0000, v167
	v_pk_mul_f32 v[118:119], v[118:119], v[150:151]
	v_cvt_pk_bf16_f32 v120, v120, v121
	v_cvt_pk_bf16_f32 v121, v122, v123
	v_cvt_pk_bf16_f32 v122, v116, v117
	v_cvt_pk_bf16_f32 v123, v118, v119
	global_store_dwordx4 v157, v[120:123], s[24:25] offset:256
	s_waitcnt vmcnt(15)
	v_lshlrev_b32_e32 v148, 16, v168
	v_and_b32_e32 v149, 0xffff0000, v168
	v_pk_mul_f32 v[112:113], v[112:113], v[148:149]
	v_lshlrev_b32_e32 v150, 16, v169
	v_and_b32_e32 v151, 0xffff0000, v169
	v_pk_mul_f32 v[114:115], v[114:115], v[150:151]
	v_lshlrev_b32_e32 v148, 16, v170
	v_and_b32_e32 v149, 0xffff0000, v170
	v_pk_mul_f32 v[108:109], v[108:109], v[148:149]
	v_lshlrev_b32_e32 v150, 16, v171
	v_and_b32_e32 v151, 0xffff0000, v171
	v_pk_mul_f32 v[110:111], v[110:111], v[150:151]
	v_cvt_pk_bf16_f32 v112, v112, v113
	v_cvt_pk_bf16_f32 v113, v114, v115
	v_cvt_pk_bf16_f32 v114, v108, v109
	v_cvt_pk_bf16_f32 v115, v110, v111
	v_add_u32_e32 v159, 0x8000, v157
	global_store_dwordx4 v159, v[112:115], s[24:25]
	s_waitcnt vmcnt(15)
	v_lshlrev_b32_e32 v148, 16, v172
	v_and_b32_e32 v149, 0xffff0000, v172
	v_pk_mul_f32 v[104:105], v[104:105], v[148:149]
	v_lshlrev_b32_e32 v150, 16, v173
	v_and_b32_e32 v151, 0xffff0000, v173
	v_pk_mul_f32 v[106:107], v[106:107], v[150:151]
	v_lshlrev_b32_e32 v148, 16, v174
	v_and_b32_e32 v149, 0xffff0000, v174
	v_pk_mul_f32 v[100:101], v[100:101], v[148:149]
	v_lshlrev_b32_e32 v150, 16, v175
	v_and_b32_e32 v151, 0xffff0000, v175
	v_pk_mul_f32 v[102:103], v[102:103], v[150:151]
	v_cvt_pk_bf16_f32 v104, v104, v105
	v_cvt_pk_bf16_f32 v105, v106, v107
	v_cvt_pk_bf16_f32 v106, v100, v101
	v_cvt_pk_bf16_f32 v107, v102, v103
	v_add_u32_e32 v159, 0x8000, v157
	global_store_dwordx4 v159, v[104:107], s[24:25] offset:256
	s_waitcnt vmcnt(15)
	v_lshlrev_b32_e32 v148, 16, v176
	v_and_b32_e32 v149, 0xffff0000, v176
	v_pk_mul_f32 v[94:95], v[94:95], v[148:149]
	v_lshlrev_b32_e32 v150, 16, v177
	v_and_b32_e32 v151, 0xffff0000, v177
	v_pk_mul_f32 v[96:97], v[96:97], v[150:151]
	v_lshlrev_b32_e32 v148, 16, v178
	v_and_b32_e32 v149, 0xffff0000, v178
	v_pk_mul_f32 v[90:91], v[90:91], v[148:149]
	v_lshlrev_b32_e32 v150, 16, v179
	v_and_b32_e32 v151, 0xffff0000, v179
	v_pk_mul_f32 v[92:93], v[92:93], v[150:151]
	v_cvt_pk_bf16_f32 v94, v94, v95
	v_cvt_pk_bf16_f32 v95, v96, v97
	v_cvt_pk_bf16_f32 v96, v90, v91
	v_cvt_pk_bf16_f32 v97, v92, v93
	v_add_u32_e32 v159, 0x10000, v157
	global_store_dwordx4 v159, v[94:97], s[24:25]
	s_waitcnt vmcnt(15)
; __device__ __forceinline__ unsigned pk2(float lo, float hi) { f32x2 v = {lo, hi}; return __builtin_bit_cast(unsigned, __builtin_convertvector(v, bf2_t)); }
; template <int BIT = 0> __device__ __forceinline__ void st16w(void* p, u32x4 v) { if ((WT_STORES >> BIT) & 1) asm volatile("global_store_dwordx4 %0, %1, off sc1\n\ts_nop 1" :: "v"(p), "v"(v) : "memory"); else *(u32x4*)p = v; }
; __device__ __forceinline__ float bflo(unsigned u) { return __uint_as_float(u << 16); }
; __device__ __forceinline__ float bfhi(unsigned u) { return __uint_as_float(u & 0xffff0000u); }
;     __device__ __forceinline__ void operator()(const f32x4 (&acc)[2][2][4][2], const Unit& u, int wr, int wc, int fr, int fq) const {
;         const int row0 = u.pm * BM + wr * 64 + fr, col0 = u.pn * BM + wc * 32 + 8 * fq;
; #pragma unroll
;         for (int ai = 0; ai < 2; ++ai)
; #pragma unroll
;             for (int m = 0; m < 4; ++m) {
;                 const size_t row = (size_t)(row0 + ai * HALF + m * 16);
; #pragma unroll
;                 for (int bj = 0; bj < 2; ++bj) {
;                     const int col = col0 + bj * HALF;
;                     const u32x4 g = *(const u32x4*)(P + row * INC + goff + col);
;                     const f32x4 a0 = acc[ai][bj][m][0], a1 = acc[ai][bj][m][1];
;                     float o[8] = {bflo(g.x) * a0[0], bfhi(g.x) * a0[1], bflo(g.y) * a0[2], bfhi(g.y) * a0[3], bflo(g.z) * a1[0], bfhi(g.z) * a1[1], bflo(g.w) * a1[2], bfhi(g.w) * a1[3]};
;                     if (mode) { const u32x4 t = *(const u32x4*)(T1 + row * D + col);
;                         o[0] += bflo(t.x); o[1] += bfhi(t.x); o[2] += bflo(t.y); o[3] += bfhi(t.y); o[4] += bflo(t.z); o[5] += bfhi(t.z); o[6] += bflo(t.w); o[7] += bfhi(t.w); }
;                     u32x4 w; w.x = pk2(o[0], o[1]); w.y = pk2(o[2], o[3]); w.z = pk2(o[4], o[5]); w.w = pk2(o[6], o[7]);
;                     if (mode) st16w(MM + row * D + col, w); else *(u32x4*)(T1 + row * D + col) = w;
	v_lshlrev_b32_e32 v148, 16, v180
	v_and_b32_e32 v149, 0xffff0000, v180
	v_pk_mul_f32 v[86:87], v[86:87], v[148:149]
	v_lshlrev_b32_e32 v150, 16, v181
	v_and_b32_e32 v151, 0xffff0000, v181
	v_pk_mul_f32 v[88:89], v[88:89], v[150:151]
	v_lshlrev_b32_e32 v148, 16, v182
	v_and_b32_e32 v149, 0xffff0000, v182
	v_pk_mul_f32 v[82:83], v[82:83], v[148:149]
	v_lshlrev_b32_e32 v150, 16, v183
	v_and_b32_e32 v151, 0xffff0000, v183
	v_pk_mul_f32 v[84:85], v[84:85], v[150:151]
	v_cvt_pk_bf16_f32 v86, v86, v87
	v_cvt_pk_bf16_f32 v87, v88, v89
	v_cvt_pk_bf16_f32 v88, v82, v83
	v_cvt_pk_bf16_f32 v89, v84, v85
	v_add_u32_e32 v159, 0x10000, v157
	global_store_dwordx4 v159, v[86:89], s[24:25] offset:256
	s_waitcnt vmcnt(15)
	v_lshlrev_b32_e32 v148, 16, v184
	v_and_b32_e32 v149, 0xffff0000, v184
	v_pk_mul_f32 v[78:79], v[78:79], v[148:149]
	v_lshlrev_b32_e32 v150, 16, v185
	v_and_b32_e32 v151, 0xffff0000, v185
	v_pk_mul_f32 v[80:81], v[80:81], v[150:151]
	v_lshlrev_b32_e32 v148, 16, v186
	v_and_b32_e32 v149, 0xffff0000, v186
	v_pk_mul_f32 v[74:75], v[74:75], v[148:149]
	v_lshlrev_b32_e32 v150, 16, v187
	v_and_b32_e32 v151, 0xffff0000, v187
	v_pk_mul_f32 v[76:77], v[76:77], v[150:151]
	v_cvt_pk_bf16_f32 v78, v78, v79
	v_cvt_pk_bf16_f32 v79, v80, v81
	v_cvt_pk_bf16_f32 v80, v74, v75
	v_cvt_pk_bf16_f32 v81, v76, v77
	v_add_u32_e32 v159, 0x18000, v157
	global_store_dwordx4 v159, v[78:81], s[24:25]
	s_waitcnt vmcnt(15)
	v_lshlrev_b32_e32 v148, 16, v188
	v_and_b32_e32 v149, 0xffff0000, v188
	v_pk_mul_f32 v[70:71], v[70:71], v[148:149]
	v_lshlrev_b32_e32 v150, 16, v189
	v_and_b32_e32 v151, 0xffff0000, v189
	v_pk_mul_f32 v[72:73], v[72:73], v[150:151]
	v_lshlrev_b32_e32 v148, 16, v190
	v_and_b32_e32 v149, 0xffff0000, v190
	v_pk_mul_f32 v[66:67], v[66:67], v[148:149]
	v_lshlrev_b32_e32 v150, 16, v191
	v_and_b32_e32 v151, 0xffff0000, v191
	v_pk_mul_f32 v[68:69], v[68:69], v[150:151]
	v_cvt_pk_bf16_f32 v70, v70, v71
	v_cvt_pk_bf16_f32 v71, v72, v73
	v_cvt_pk_bf16_f32 v72, v66, v67
	v_cvt_pk_bf16_f32 v73, v68, v69
	v_add_u32_e32 v159, 0x18000, v157
	global_store_dwordx4 v159, v[70:73], s[24:25] offset:256
	s_waitcnt vmcnt(15)
	v_lshlrev_b32_e32 v148, 16, v192
	v_and_b32_e32 v149, 0xffff0000, v192
	v_pk_mul_f32 v[62:63], v[62:63], v[148:149]
	v_lshlrev_b32_e32 v150, 16, v193
	v_and_b32_e32 v151, 0xffff0000, v193
	v_pk_mul_f32 v[64:65], v[64:65], v[150:151]
	v_lshlrev_b32_e32 v148, 16, v194
	v_and_b32_e32 v149, 0xffff0000, v194
	v_pk_mul_f32 v[58:59], v[58:59], v[148:149]
	v_lshlrev_b32_e32 v150, 16, v195
	v_and_b32_e32 v151, 0xffff0000, v195
	v_pk_mul_f32 v[60:61], v[60:61], v[150:151]
	v_cvt_pk_bf16_f32 v62, v62, v63
	v_cvt_pk_bf16_f32 v63, v64, v65
	v_cvt_pk_bf16_f32 v64, v58, v59
	v_cvt_pk_bf16_f32 v65, v60, v61
	v_add_u32_e32 v159, 0x40000, v157
	global_store_dwordx4 v159, v[62:65], s[24:25]
	s_waitcnt vmcnt(15)
	v_lshlrev_b32_e32 v148, 16, v196
	v_and_b32_e32 v149, 0xffff0000, v196
	v_pk_mul_f32 v[54:55], v[54:55], v[148:149]
	v_lshlrev_b32_e32 v150, 16, v197
	v_and_b32_e32 v151, 0xffff0000, v197
	v_pk_mul_f32 v[56:57], v[56:57], v[150:151]
	v_lshlrev_b32_e32 v148, 16, v198
	v_and_b32_e32 v149, 0xffff0000, v198
	v_pk_mul_f32 v[50:51], v[50:51], v[148:149]
	v_lshlrev_b32_e32 v150, 16, v199
	v_and_b32_e32 v151, 0xffff0000, v199
	v_pk_mul_f32 v[52:53], v[52:53], v[150:151]
	v_cvt_pk_bf16_f32 v54, v54, v55
	v_cvt_pk_bf16_f32 v55, v56, v57
	v_cvt_pk_bf16_f32 v56, v50, v51
	v_cvt_pk_bf16_f32 v57, v52, v53
	v_add_u32_e32 v159, 0x40000, v157
	global_store_dwordx4 v159, v[54:57], s[24:25] offset:256
	s_waitcnt vmcnt(15)
	v_lshlrev_b32_e32 v148, 16, v208
	v_and_b32_e32 v149, 0xffff0000, v208
	v_pk_mul_f32 v[46:47], v[46:47], v[148:149]
	v_lshlrev_b32_e32 v150, 16, v209
	v_and_b32_e32 v151, 0xffff0000, v209
	v_pk_mul_f32 v[48:49], v[48:49], v[150:151]
	v_lshlrev_b32_e32 v148, 16, v210
	v_and_b32_e32 v149, 0xffff0000, v210
	v_pk_mul_f32 v[42:43], v[42:43], v[148:149]
	v_lshlrev_b32_e32 v150, 16, v211
	v_and_b32_e32 v151, 0xffff0000, v211
	v_pk_mul_f32 v[44:45], v[44:45], v[150:151]
	v_cvt_pk_bf16_f32 v46, v46, v47
	v_cvt_pk_bf16_f32 v47, v48, v49
	v_cvt_pk_bf16_f32 v48, v42, v43
	v_cvt_pk_bf16_f32 v49, v44, v45
	v_add_u32_e32 v159, 0x48000, v157
	global_store_dwordx4 v159, v[46:49], s[24:25]
	s_waitcnt vmcnt(15)
; __device__ __forceinline__ unsigned pk2(float lo, float hi) { f32x2 v = {lo, hi}; return __builtin_bit_cast(unsigned, __builtin_convertvector(v, bf2_t)); }
; template <int BIT = 0> __device__ __forceinline__ void st16w(void* p, u32x4 v) { if ((WT_STORES >> BIT) & 1) asm volatile("global_store_dwordx4 %0, %1, off sc1\n\ts_nop 1" :: "v"(p), "v"(v) : "memory"); else *(u32x4*)p = v; }
; __device__ __forceinline__ float bflo(unsigned u) { return __uint_as_float(u << 16); }
; __device__ __forceinline__ float bfhi(unsigned u) { return __uint_as_float(u & 0xffff0000u); }
;     __device__ __forceinline__ void operator()(const f32x4 (&acc)[2][2][4][2], const Unit& u, int wr, int wc, int fr, int fq) const {
;         const int row0 = u.pm * BM + wr * 64 + fr, col0 = u.pn * BM + wc * 32 + 8 * fq;
; #pragma unroll
;         for (int ai = 0; ai < 2; ++ai)
; #pragma unroll
;             for (int m = 0; m < 4; ++m) {
;                 const size_t row = (size_t)(row0 + ai * HALF + m * 16);
; #pragma unroll
;                 for (int bj = 0; bj < 2; ++bj) {
;                     const int col = col0 + bj * HALF;
;                     const u32x4 g = *(const u32x4*)(P + row * INC + goff + col);
;                     const f32x4 a0 = acc[ai][bj][m][0], a1 = acc[ai][bj][m][1];
;                     float o[8] = {bflo(g.x) * a0[0], bfhi(g.x) * a0[1], bflo(g.y) * a0[2], bfhi(g.y) * a0[3], bflo(g.z) * a1[0], bfhi(g.z) * a1[1], bflo(g.w) * a1[2], bfhi(g.w) * a1[3]};
;                     if (mode) { const u32x4 t = *(const u32x4*)(T1 + row * D + col);
;                         o[0] += bflo(t.x); o[1] += bfhi(t.x); o[2] += bflo(t.y); o[3] += bfhi(t.y); o[4] += bflo(t.z); o[5] += bfhi(t.z); o[6] += bflo(t.w); o[7] += bfhi(t.w); }
;                     u32x4 w; w.x = pk2(o[0], o[1]); w.y = pk2(o[2], o[3]); w.z = pk2(o[4], o[5]); w.w = pk2(o[6], o[7]);
;                     if (mode) st16w(MM + row * D + col, w); else *(u32x4*)(T1 + row * D + col) = w;
	v_lshlrev_b32_e32 v148, 16, v212
	v_and_b32_e32 v149, 0xffff0000, v212
	v_pk_mul_f32 v[38:39], v[38:39], v[148:149]
	v_lshlrev_b32_e32 v150, 16, v213
	v_and_b32_e32 v151, 0xffff0000, v213
	v_pk_mul_f32 v[40:41], v[40:41], v[150:151]
	v_lshlrev_b32_e32 v148, 16, v214
	v_and_b32_e32 v149, 0xffff0000, v214
	v_pk_mul_f32 v[34:35], v[34:35], v[148:149]
	v_lshlrev_b32_e32 v150, 16, v215
	v_and_b32_e32 v151, 0xffff0000, v215
	v_pk_mul_f32 v[36:37], v[36:37], v[150:151]
	v_cvt_pk_bf16_f32 v38, v38, v39
	v_cvt_pk_bf16_f32 v39, v40, v41
	v_cvt_pk_bf16_f32 v40, v34, v35
	v_cvt_pk_bf16_f32 v41, v36, v37
	v_add_u32_e32 v159, 0x48000, v157
	global_store_dwordx4 v159, v[38:41], s[24:25] offset:256
	s_waitcnt vmcnt(15)
	v_lshlrev_b32_e32 v148, 16, v216
	v_and_b32_e32 v149, 0xffff0000, v216
	v_pk_mul_f32 v[30:31], v[30:31], v[148:149]
	v_lshlrev_b32_e32 v150, 16, v217
	v_and_b32_e32 v151, 0xffff0000, v217
	v_pk_mul_f32 v[32:33], v[32:33], v[150:151]
	v_lshlrev_b32_e32 v148, 16, v218
	v_and_b32_e32 v149, 0xffff0000, v218
	v_pk_mul_f32 v[26:27], v[26:27], v[148:149]
	v_lshlrev_b32_e32 v150, 16, v219
	v_and_b32_e32 v151, 0xffff0000, v219
	v_pk_mul_f32 v[28:29], v[28:29], v[150:151]
	v_cvt_pk_bf16_f32 v30, v30, v31
	v_cvt_pk_bf16_f32 v31, v32, v33
	v_cvt_pk_bf16_f32 v32, v26, v27
	v_cvt_pk_bf16_f32 v33, v28, v29
	v_add_u32_e32 v159, 0x50000, v157
	global_store_dwordx4 v159, v[30:33], s[24:25]
	s_waitcnt vmcnt(15)
	v_lshlrev_b32_e32 v148, 16, v220
	v_and_b32_e32 v149, 0xffff0000, v220
	v_pk_mul_f32 v[22:23], v[22:23], v[148:149]
	v_lshlrev_b32_e32 v150, 16, v221
	v_and_b32_e32 v151, 0xffff0000, v221
	v_pk_mul_f32 v[24:25], v[24:25], v[150:151]
	v_lshlrev_b32_e32 v148, 16, v222
	v_and_b32_e32 v149, 0xffff0000, v222
	v_pk_mul_f32 v[18:19], v[18:19], v[148:149]
	v_lshlrev_b32_e32 v150, 16, v223
	v_and_b32_e32 v151, 0xffff0000, v223
	v_pk_mul_f32 v[20:21], v[20:21], v[150:151]
	v_cvt_pk_bf16_f32 v22, v22, v23
	v_cvt_pk_bf16_f32 v23, v24, v25
	v_cvt_pk_bf16_f32 v24, v18, v19
	v_cvt_pk_bf16_f32 v25, v20, v21
	v_add_u32_e32 v159, 0x50000, v157
	global_store_dwordx4 v159, v[22:25], s[24:25] offset:256
	s_waitcnt vmcnt(14)
	v_lshlrev_b32_e32 v148, 16, v160
	v_and_b32_e32 v149, 0xffff0000, v160
	v_pk_mul_f32 v[14:15], v[14:15], v[148:149]
	v_lshlrev_b32_e32 v150, 16, v161
	v_and_b32_e32 v151, 0xffff0000, v161
	v_pk_mul_f32 v[16:17], v[16:17], v[150:151]
	v_lshlrev_b32_e32 v148, 16, v162
	v_and_b32_e32 v149, 0xffff0000, v162
	v_pk_mul_f32 v[10:11], v[10:11], v[148:149]
	v_lshlrev_b32_e32 v150, 16, v163
	v_and_b32_e32 v151, 0xffff0000, v163
	v_pk_mul_f32 v[12:13], v[12:13], v[150:151]
	v_cvt_pk_bf16_f32 v14, v14, v15
	v_cvt_pk_bf16_f32 v15, v16, v17
	v_cvt_pk_bf16_f32 v16, v10, v11
	v_cvt_pk_bf16_f32 v17, v12, v13
	v_add_u32_e32 v159, 0x58000, v157
	global_store_dwordx4 v159, v[14:17], s[24:25]
	s_waitcnt vmcnt(14)
	v_lshlrev_b32_e32 v148, 16, v124
	v_and_b32_e32 v149, 0xffff0000, v124
	v_pk_mul_f32 v[6:7], v[6:7], v[148:149]
	v_lshlrev_b32_e32 v150, 16, v125
	v_and_b32_e32 v151, 0xffff0000, v125
	v_pk_mul_f32 v[8:9], v[8:9], v[150:151]
	v_lshlrev_b32_e32 v148, 16, v126
	v_and_b32_e32 v149, 0xffff0000, v126
	v_pk_mul_f32 v[2:3], v[2:3], v[148:149]
	v_lshlrev_b32_e32 v150, 16, v127
	v_and_b32_e32 v151, 0xffff0000, v127
	v_pk_mul_f32 v[4:5], v[4:5], v[150:151]
	v_cvt_pk_bf16_f32 v6, v6, v7
	v_cvt_pk_bf16_f32 v7, v8, v9
	v_cvt_pk_bf16_f32 v8, v2, v3
	v_cvt_pk_bf16_f32 v9, v4, v5
	v_add_u32_e32 v159, 0x58000, v157
	global_store_dwordx4 v159, v[6:9], s[24:25] offset:256
	s_nop 1
	s_mov_b64 s[24:25], 0x2400
	s_cbranch_vccnz .LBB13_814
	s_andn2_b64 vcc, exec, s[6:7]
	s_cbranch_vccnz .LBB13_813
	s_barrier
	s_branch .LBB13_813

; __device__ __forceinline__ unsigned pk2(float lo, float hi) { f32x2 v = {lo, hi}; return __builtin_bit_cast(unsigned, __builtin_convertvector(v, bf2_t)); }
; template <int BIT = 0> __device__ __forceinline__ void st16w(void* p, u32x4 v) { if ((WT_STORES >> BIT) & 1) asm volatile("global_store_dwordx4 %0, %1, off sc1\n\ts_nop 1" :: "v"(p), "v"(v) : "memory"); else *(u32x4*)p = v; }
; __device__ __forceinline__ float bflo(unsigned u) { return __uint_as_float(u << 16); }
; __device__ __forceinline__ float bfhi(unsigned u) { return __uint_as_float(u & 0xffff0000u); }
;     __device__ __forceinline__ void operator()(const f32x4 (&acc)[2][2][4][2], const Unit& u, int wr, int wc, int fr, int fq) const {
;         const int row0 = u.pm * BM + wr * 64 + fr, col0 = u.pn * BM + wc * 32 + 8 * fq;
; #pragma unroll
;         for (int ai = 0; ai < 2; ++ai)
; #pragma unroll
;             for (int m = 0; m < 4; ++m) {
;                 const size_t row = (size_t)(row0 + ai * HALF + m * 16);
; #pragma unroll
;                 for (int bj = 0; bj < 2; ++bj) {
;                     const int col = col0 + bj * HALF;
;                     const u32x4 g = *(const u32x4*)(P + row * INC + goff + col);
;                     const f32x4 a0 = acc[ai][bj][m][0], a1 = acc[ai][bj][m][1];
;                     float o[8] = {bflo(g.x) * a0[0], bfhi(g.x) * a0[1], bflo(g.y) * a0[2], bfhi(g.y) * a0[3], bflo(g.z) * a1[0], bfhi(g.z) * a1[1], bflo(g.w) * a1[2], bfhi(g.w) * a1[3]};
;                     if (mode) { const u32x4 t = *(const u32x4*)(T1 + row * D + col);
;                         o[0] += bflo(t.x); o[1] += bfhi(t.x); o[2] += bflo(t.y); o[3] += bfhi(t.y); o[4] += bflo(t.z); o[5] += bfhi(t.z); o[6] += bflo(t.w); o[7] += bfhi(t.w); }
;                     u32x4 w; w.x = pk2(o[0], o[1]); w.y = pk2(o[2], o[3]); w.z = pk2(o[4], o[5]); w.w = pk2(o[6], o[7]);
;                     if (mode) st16w(MM + row * D + col, w); else *(u32x4*)(T1 + row * D + col) = w;
.LBB13_847:
	v_readfirstlane_b32 s98, v132
	v_readfirstlane_b32 s99, v133
	v_readfirstlane_b32 s22, v134
	v_readfirstlane_b32 s23, v135
	v_lshl_add_u32 v158, s12, 8, v99
	v_lshl_or_b32 v159, s13, 8, v153
	s_mov_b64 s[12:13], -1
	s_andn2_b64 vcc, exec, s[4:5]
	v_mul_u32_u24_e32 v156, 0x2c00, v158
	v_lshl_add_u32 v156, v159, 1, v156
	v_add_u32_e32 v156, 0x1c00, v156
	v_lshlrev_b32_e32 v157, 11, v158
	v_lshl_add_u32 v157, v159, 1, v157
	global_load_dwordx4 v[160:163], v156, s[98:99]
	global_load_dwordx4 v[164:167], v157, s[22:23]
	global_load_dwordx4 v[168:171], v156, s[98:99] offset:256
	global_load_dwordx4 v[172:175], v157, s[22:23] offset:256
	v_add_u32_e32 v158, 0x2c000, v156
	global_load_dwordx4 v[176:179], v158, s[98:99]
	v_add_u32_e32 v159, 0x8000, v157
	global_load_dwordx4 v[180:183], v159, s[22:23]
	v_add_u32_e32 v158, 0x2c000, v156
	global_load_dwordx4 v[184:187], v158, s[98:99] offset:256
	v_add_u32_e32 v159, 0x8000, v157
	global_load_dwordx4 v[188:191], v159, s[22:23] offset:256
	v_add_u32_e32 v158, 0x58000, v156
	global_load_dwordx4 v[192:195], v158, s[98:99]
	v_add_u32_e32 v159, 0x10000, v157
	global_load_dwordx4 v[196:199], v159, s[22:23]
	v_add_u32_e32 v158, 0x58000, v156
	global_load_dwordx4 v[208:211], v158, s[98:99] offset:256
	v_add_u32_e32 v159, 0x10000, v157
	global_load_dwordx4 v[212:215], v159, s[22:23] offset:256
	v_add_u32_e32 v158, 0x84000, v156
	global_load_dwordx4 v[216:219], v158, s[98:99]
	v_add_u32_e32 v159, 0x18000, v157
	global_load_dwordx4 v[220:223], v159, s[22:23]
	s_waitcnt vmcnt(12)
	v_lshlrev_b32_e32 v148, 16, v160
	v_and_b32_e32 v149, 0xffff0000, v160
	v_lshlrev_b32_e32 v150, 16, v164
	v_and_b32_e32 v151, 0xffff0000, v164
	v_pk_fma_f32 v[128:129], v[128:129], v[148:149], v[150:151]
	v_lshlrev_b32_e32 v148, 16, v161
	v_and_b32_e32 v149, 0xffff0000, v161
	v_lshlrev_b32_e32 v150, 16, v165
	v_and_b32_e32 v151, 0xffff0000, v165
	v_pk_fma_f32 v[130:131], v[130:131], v[148:149], v[150:151]
	v_lshlrev_b32_e32 v148, 16, v162
	v_and_b32_e32 v149, 0xffff0000, v162
	v_lshlrev_b32_e32 v150, 16, v166
	v_and_b32_e32 v151, 0xffff0000, v166
	v_pk_fma_f32 v[124:125], v[124:125], v[148:149], v[150:151]
	v_lshlrev_b32_e32 v148, 16, v163
	v_and_b32_e32 v149, 0xffff0000, v163
	v_lshlrev_b32_e32 v150, 16, v167
	v_and_b32_e32 v151, 0xffff0000, v167
	v_pk_fma_f32 v[126:127], v[126:127], v[148:149], v[150:151]
	v_cvt_pk_bf16_f32 v128, v128, v129
	v_cvt_pk_bf16_f32 v129, v130, v131
	v_cvt_pk_bf16_f32 v130, v124, v125
	v_cvt_pk_bf16_f32 v131, v126, v127
	global_store_dwordx4 v157, v[128:131], s[6:7]
	v_add_u32_e32 v158, 0x84000, v156
	global_load_dwordx4 v[160:163], v158, s[98:99] offset:256
	v_add_u32_e32 v159, 0x18000, v157
	global_load_dwordx4 v[164:167], v159, s[22:23] offset:256
	s_waitcnt vmcnt(13)
	v_lshlrev_b32_e32 v148, 16, v168
	v_and_b32_e32 v149, 0xffff0000, v168
	v_lshlrev_b32_e32 v150, 16, v172
	v_and_b32_e32 v151, 0xffff0000, v172
	v_pk_fma_f32 v[120:121], v[120:121], v[148:149], v[150:151]
	v_lshlrev_b32_e32 v148, 16, v169
	v_and_b32_e32 v149, 0xffff0000, v169
	v_lshlrev_b32_e32 v150, 16, v173
	v_and_b32_e32 v151, 0xffff0000, v173
	v_pk_fma_f32 v[122:123], v[122:123], v[148:149], v[150:151]
	v_lshlrev_b32_e32 v148, 16, v170
	v_and_b32_e32 v149, 0xffff0000, v170
	v_lshlrev_b32_e32 v150, 16, v174
	v_and_b32_e32 v151, 0xffff0000, v174
	v_pk_fma_f32 v[116:117], v[116:117], v[148:149], v[150:151]
	v_lshlrev_b32_e32 v148, 16, v171
	v_and_b32_e32 v149, 0xffff0000, v171
	v_lshlrev_b32_e32 v150, 16, v175
	v_and_b32_e32 v151, 0xffff0000, v175
	v_pk_fma_f32 v[118:119], v[118:119], v[148:149], v[150:151]
	v_cvt_pk_bf16_f32 v120, v120, v121
	v_cvt_pk_bf16_f32 v121, v122, v123
	v_cvt_pk_bf16_f32 v122, v116, v117
	v_cvt_pk_bf16_f32 v123, v118, v119
	global_store_dwordx4 v157, v[120:123], s[6:7] offset:256
	v_add_u32_e32 v158, 0x160000, v156
	global_load_dwordx4 v[124:127], v158, s[98:99]
	v_add_u32_e32 v159, 0x40000, v157
	global_load_dwordx4 v[168:171], v159, s[22:23]
	v_add_u32_e32 v158, 0x160000, v156
	global_load_dwordx4 v[172:175], v158, s[98:99] offset:256
	v_add_u32_e32 v159, 0x40000, v157
	global_load_dwordx4 v[116:119], v159, s[22:23] offset:256
	s_waitcnt vmcnt(16)
	v_lshlrev_b32_e32 v148, 16, v176
	v_and_b32_e32 v149, 0xffff0000, v176
	v_lshlrev_b32_e32 v150, 16, v180
	v_and_b32_e32 v151, 0xffff0000, v180
	v_pk_fma_f32 v[112:113], v[112:113], v[148:149], v[150:151]
	v_lshlrev_b32_e32 v148, 16, v177
	v_and_b32_e32 v149, 0xffff0000, v177
	v_lshlrev_b32_e32 v150, 16, v181
	v_and_b32_e32 v151, 0xffff0000, v181
	v_pk_fma_f32 v[114:115], v[114:115], v[148:149], v[150:151]
	v_lshlrev_b32_e32 v148, 16, v178
	v_and_b32_e32 v149, 0xffff0000, v178
	v_lshlrev_b32_e32 v150, 16, v182
	v_and_b32_e32 v151, 0xffff0000, v182
	v_pk_fma_f32 v[108:109], v[108:109], v[148:149], v[150:151]
	v_lshlrev_b32_e32 v148, 16, v179
	v_and_b32_e32 v149, 0xffff0000, v179
	v_lshlrev_b32_e32 v150, 16, v183
	v_and_b32_e32 v151, 0xffff0000, v183
	v_pk_fma_f32 v[110:111], v[110:111], v[148:149], v[150:151]
	v_cvt_pk_bf16_f32 v112, v112, v113
	v_cvt_pk_bf16_f32 v113, v114, v115
	v_cvt_pk_bf16_f32 v114, v108, v109
	v_cvt_pk_bf16_f32 v115, v110, v111
	v_add_u32_e32 v159, 0x8000, v157
	global_store_dwordx4 v159, v[112:115], s[6:7]
	v_add_u32_e32 v158, 0x18c000, v156
	global_load_dwordx4 v[176:179], v158, s[98:99]
	v_add_u32_e32 v159, 0x48000, v157
	global_load_dwordx4 v[180:183], v159, s[22:23]
	s_waitcnt vmcnt(17)
; __device__ __forceinline__ unsigned pk2(float lo, float hi) { f32x2 v = {lo, hi}; return __builtin_bit_cast(unsigned, __builtin_convertvector(v, bf2_t)); }
; template <int BIT = 0> __device__ __forceinline__ void st16w(void* p, u32x4 v) { if ((WT_STORES >> BIT) & 1) asm volatile("global_store_dwordx4 %0, %1, off sc1\n\ts_nop 1" :: "v"(p), "v"(v) : "memory"); else *(u32x4*)p = v; }
; __device__ __forceinline__ float bflo(unsigned u) { return __uint_as_float(u << 16); }
; __device__ __forceinline__ float bfhi(unsigned u) { return __uint_as_float(u & 0xffff0000u); }
;     __device__ __forceinline__ void operator()(const f32x4 (&acc)[2][2][4][2], const Unit& u, int wr, int wc, int fr, int fq) const {
;         const int row0 = u.pm * BM + wr * 64 + fr, col0 = u.pn * BM + wc * 32 + 8 * fq;
; #pragma unroll
;         for (int ai = 0; ai < 2; ++ai)
; #pragma unroll
;             for (int m = 0; m < 4; ++m) {
;                 const size_t row = (size_t)(row0 + ai * HALF + m * 16);
; #pragma unroll
;                 for (int bj = 0; bj < 2; ++bj) {
;                     const int col = col0 + bj * HALF;
;                     const u32x4 g = *(const u32x4*)(P + row * INC + goff + col);
;                     const f32x4 a0 = acc[ai][bj][m][0], a1 = acc[ai][bj][m][1];
;                     float o[8] = {bflo(g.x) * a0[0], bfhi(g.x) * a0[1], bflo(g.y) * a0[2], bfhi(g.y) * a0[3], bflo(g.z) * a1[0], bfhi(g.z) * a1[1], bflo(g.w) * a1[2], bfhi(g.w) * a1[3]};
;                     if (mode) { const u32x4 t = *(const u32x4*)(T1 + row * D + col);
;                         o[0] += bflo(t.x); o[1] += bfhi(t.x); o[2] += bflo(t.y); o[3] += bfhi(t.y); o[4] += bflo(t.z); o[5] += bfhi(t.z); o[6] += bflo(t.w); o[7] += bfhi(t.w); }
;                     u32x4 w; w.x = pk2(o[0], o[1]); w.y = pk2(o[2], o[3]); w.z = pk2(o[4], o[5]); w.w = pk2(o[6], o[7]);
;                     if (mode) st16w(MM + row * D + col, w); else *(u32x4*)(T1 + row * D + col) = w;
	v_lshlrev_b32_e32 v148, 16, v184
	v_and_b32_e32 v149, 0xffff0000, v184
	v_lshlrev_b32_e32 v150, 16, v188
	v_and_b32_e32 v151, 0xffff0000, v188
	v_pk_fma_f32 v[104:105], v[104:105], v[148:149], v[150:151]
	v_lshlrev_b32_e32 v148, 16, v185
	v_and_b32_e32 v149, 0xffff0000, v185
	v_lshlrev_b32_e32 v150, 16, v189
	v_and_b32_e32 v151, 0xffff0000, v189
	v_pk_fma_f32 v[106:107], v[106:107], v[148:149], v[150:151]
	v_lshlrev_b32_e32 v148, 16, v186
	v_and_b32_e32 v149, 0xffff0000, v186
	v_lshlrev_b32_e32 v150, 16, v190
	v_and_b32_e32 v151, 0xffff0000, v190
	v_pk_fma_f32 v[100:101], v[100:101], v[148:149], v[150:151]
	v_lshlrev_b32_e32 v148, 16, v187
	v_and_b32_e32 v149, 0xffff0000, v187
	v_lshlrev_b32_e32 v150, 16, v191
	v_and_b32_e32 v151, 0xffff0000, v191
	v_pk_fma_f32 v[102:103], v[102:103], v[148:149], v[150:151]
	v_cvt_pk_bf16_f32 v104, v104, v105
	v_cvt_pk_bf16_f32 v105, v106, v107
	v_cvt_pk_bf16_f32 v106, v100, v101
	v_cvt_pk_bf16_f32 v107, v102, v103
	v_add_u32_e32 v159, 0x8000, v157
	global_store_dwordx4 v159, v[104:107], s[6:7] offset:256
	v_add_u32_e32 v158, 0x18c000, v156
	global_load_dwordx4 v[108:111], v158, s[98:99] offset:256
	v_add_u32_e32 v159, 0x48000, v157
	global_load_dwordx4 v[184:187], v159, s[22:23] offset:256
	v_add_u32_e32 v158, 0x1b8000, v156
	global_load_dwordx4 v[188:191], v158, s[98:99]
	v_add_u32_e32 v159, 0x50000, v157
	global_load_dwordx4 v[100:103], v159, s[22:23]
	s_waitcnt vmcnt(20)
	v_lshlrev_b32_e32 v148, 16, v192
	v_and_b32_e32 v149, 0xffff0000, v192
	v_lshlrev_b32_e32 v150, 16, v196
	v_and_b32_e32 v151, 0xffff0000, v196
	v_pk_fma_f32 v[94:95], v[94:95], v[148:149], v[150:151]
	v_lshlrev_b32_e32 v148, 16, v193
	v_and_b32_e32 v149, 0xffff0000, v193
	v_lshlrev_b32_e32 v150, 16, v197
	v_and_b32_e32 v151, 0xffff0000, v197
	v_pk_fma_f32 v[96:97], v[96:97], v[148:149], v[150:151]
	v_lshlrev_b32_e32 v148, 16, v194
	v_and_b32_e32 v149, 0xffff0000, v194
	v_lshlrev_b32_e32 v150, 16, v198
	v_and_b32_e32 v151, 0xffff0000, v198
	v_pk_fma_f32 v[90:91], v[90:91], v[148:149], v[150:151]
	v_lshlrev_b32_e32 v148, 16, v195
	v_and_b32_e32 v149, 0xffff0000, v195
	v_lshlrev_b32_e32 v150, 16, v199
	v_and_b32_e32 v151, 0xffff0000, v199
	v_pk_fma_f32 v[92:93], v[92:93], v[148:149], v[150:151]
	v_cvt_pk_bf16_f32 v94, v94, v95
	v_cvt_pk_bf16_f32 v95, v96, v97
	v_cvt_pk_bf16_f32 v96, v90, v91
	v_cvt_pk_bf16_f32 v97, v92, v93
	v_add_u32_e32 v159, 0x10000, v157
	global_store_dwordx4 v159, v[94:97], s[6:7]
	v_add_u32_e32 v158, 0x1b8000, v156
	global_load_dwordx4 v[192:195], v158, s[98:99] offset:256
	v_add_u32_e32 v159, 0x50000, v157
	global_load_dwordx4 v[196:199], v159, s[22:23] offset:256
	s_waitcnt vmcnt(21)
	v_lshlrev_b32_e32 v148, 16, v208
	v_and_b32_e32 v149, 0xffff0000, v208
	v_lshlrev_b32_e32 v150, 16, v212
	v_and_b32_e32 v151, 0xffff0000, v212
	v_pk_fma_f32 v[86:87], v[86:87], v[148:149], v[150:151]
	v_lshlrev_b32_e32 v148, 16, v209
	v_and_b32_e32 v149, 0xffff0000, v209
	v_lshlrev_b32_e32 v150, 16, v213
	v_and_b32_e32 v151, 0xffff0000, v213
	v_pk_fma_f32 v[88:89], v[88:89], v[148:149], v[150:151]
	v_lshlrev_b32_e32 v148, 16, v210
	v_and_b32_e32 v149, 0xffff0000, v210
	v_lshlrev_b32_e32 v150, 16, v214
	v_and_b32_e32 v151, 0xffff0000, v214
	v_pk_fma_f32 v[82:83], v[82:83], v[148:149], v[150:151]
	v_lshlrev_b32_e32 v148, 16, v211
	v_and_b32_e32 v149, 0xffff0000, v211
	v_lshlrev_b32_e32 v150, 16, v215
	v_and_b32_e32 v151, 0xffff0000, v215
	v_pk_fma_f32 v[84:85], v[84:85], v[148:149], v[150:151]
	v_cvt_pk_bf16_f32 v86, v86, v87
	v_cvt_pk_bf16_f32 v87, v88, v89
	v_cvt_pk_bf16_f32 v88, v82, v83
	v_cvt_pk_bf16_f32 v89, v84, v85
	v_add_u32_e32 v159, 0x10000, v157
	global_store_dwordx4 v159, v[86:89], s[6:7] offset:256
	v_add_u32_e32 v158, 0x1e4000, v156
	global_load_dwordx4 v[90:93], v158, s[98:99]
	v_add_u32_e32 v159, 0x58000, v157
	global_load_dwordx4 v[208:211], v159, s[22:23]
	v_add_u32_e32 v158, 0x1e4000, v156
	global_load_dwordx4 v[212:215], v158, s[98:99] offset:256
	v_add_u32_e32 v159, 0x58000, v157
	global_load_dwordx4 v[82:85], v159, s[22:23] offset:256
	s_waitcnt vmcnt(24)
	v_lshlrev_b32_e32 v148, 16, v216
	v_and_b32_e32 v149, 0xffff0000, v216
	v_lshlrev_b32_e32 v150, 16, v220
	v_and_b32_e32 v151, 0xffff0000, v220
	v_pk_fma_f32 v[78:79], v[78:79], v[148:149], v[150:151]
	v_lshlrev_b32_e32 v148, 16, v217
	v_and_b32_e32 v149, 0xffff0000, v217
	v_lshlrev_b32_e32 v150, 16, v221
	v_and_b32_e32 v151, 0xffff0000, v221
	v_pk_fma_f32 v[80:81], v[80:81], v[148:149], v[150:151]
	v_lshlrev_b32_e32 v148, 16, v218
	v_and_b32_e32 v149, 0xffff0000, v218
	v_lshlrev_b32_e32 v150, 16, v222
	v_and_b32_e32 v151, 0xffff0000, v222
	v_pk_fma_f32 v[74:75], v[74:75], v[148:149], v[150:151]
	v_lshlrev_b32_e32 v148, 16, v219
	v_and_b32_e32 v149, 0xffff0000, v219
	v_lshlrev_b32_e32 v150, 16, v223
	v_and_b32_e32 v151, 0xffff0000, v223
	v_pk_fma_f32 v[76:77], v[76:77], v[148:149], v[150:151]
	v_cvt_pk_bf16_f32 v78, v78, v79
	v_cvt_pk_bf16_f32 v79, v80, v81
	v_cvt_pk_bf16_f32 v80, v74, v75
	v_cvt_pk_bf16_f32 v81, v76, v77
	v_add_u32_e32 v159, 0x18000, v157
	global_store_dwordx4 v159, v[78:81], s[6:7]
	s_waitcnt vmcnt(22)
	v_lshlrev_b32_e32 v148, 16, v160
	v_and_b32_e32 v149, 0xffff0000, v160
	v_lshlrev_b32_e32 v150, 16, v164
	v_and_b32_e32 v151, 0xffff0000, v164
	v_pk_fma_f32 v[70:71], v[70:71], v[148:149], v[150:151]
	v_lshlrev_b32_e32 v148, 16, v161
	v_and_b32_e32 v149, 0xffff0000, v161
	v_lshlrev_b32_e32 v150, 16, v165
	v_and_b32_e32 v151, 0xffff0000, v165
	v_pk_fma_f32 v[72:73], v[72:73], v[148:149], v[150:151]
	v_lshlrev_b32_e32 v148, 16, v162
	v_and_b32_e32 v149, 0xffff0000, v162
	v_lshlrev_b32_e32 v150, 16, v166
	v_and_b32_e32 v151, 0xffff0000, v166
	v_pk_fma_f32 v[66:67], v[66:67], v[148:149], v[150:151]
	v_lshlrev_b32_e32 v148, 16, v163
	v_and_b32_e32 v149, 0xffff0000, v163
	v_lshlrev_b32_e32 v150, 16, v167
	v_and_b32_e32 v151, 0xffff0000, v167
	v_pk_fma_f32 v[68:69], v[68:69], v[148:149], v[150:151]
	v_cvt_pk_bf16_f32 v70, v70, v71
	v_cvt_pk_bf16_f32 v71, v72, v73
	v_cvt_pk_bf16_f32 v72, v66, v67
	v_cvt_pk_bf16_f32 v73, v68, v69
	v_add_u32_e32 v159, 0x18000, v157
	global_store_dwordx4 v159, v[70:73], s[6:7] offset:256
	s_waitcnt vmcnt(20)
; __device__ __forceinline__ unsigned pk2(float lo, float hi) { f32x2 v = {lo, hi}; return __builtin_bit_cast(unsigned, __builtin_convertvector(v, bf2_t)); }
; template <int BIT = 0> __device__ __forceinline__ void st16w(void* p, u32x4 v) { if ((WT_STORES >> BIT) & 1) asm volatile("global_store_dwordx4 %0, %1, off sc1\n\ts_nop 1" :: "v"(p), "v"(v) : "memory"); else *(u32x4*)p = v; }
; __device__ __forceinline__ float bflo(unsigned u) { return __uint_as_float(u << 16); }
; __device__ __forceinline__ float bfhi(unsigned u) { return __uint_as_float(u & 0xffff0000u); }
;     __device__ __forceinline__ void operator()(const f32x4 (&acc)[2][2][4][2], const Unit& u, int wr, int wc, int fr, int fq) const {
;         const int row0 = u.pm * BM + wr * 64 + fr, col0 = u.pn * BM + wc * 32 + 8 * fq;
; #pragma unroll
;         for (int ai = 0; ai < 2; ++ai)
; #pragma unroll
;             for (int m = 0; m < 4; ++m) {
;                 const size_t row = (size_t)(row0 + ai * HALF + m * 16);
; #pragma unroll
;                 for (int bj = 0; bj < 2; ++bj) {
;                     const int col = col0 + bj * HALF;
;                     const u32x4 g = *(const u32x4*)(P + row * INC + goff + col);
;                     const f32x4 a0 = acc[ai][bj][m][0], a1 = acc[ai][bj][m][1];
;                     float o[8] = {bflo(g.x) * a0[0], bfhi(g.x) * a0[1], bflo(g.y) * a0[2], bfhi(g.y) * a0[3], bflo(g.z) * a1[0], bfhi(g.z) * a1[1], bflo(g.w) * a1[2], bfhi(g.w) * a1[3]};
;                     if (mode) { const u32x4 t = *(const u32x4*)(T1 + row * D + col);
;                         o[0] += bflo(t.x); o[1] += bfhi(t.x); o[2] += bflo(t.y); o[3] += bfhi(t.y); o[4] += bflo(t.z); o[5] += bfhi(t.z); o[6] += bflo(t.w); o[7] += bfhi(t.w); }
;                     u32x4 w; w.x = pk2(o[0], o[1]); w.y = pk2(o[2], o[3]); w.z = pk2(o[4], o[5]); w.w = pk2(o[6], o[7]);
;                     if (mode) st16w(MM + row * D + col, w); else *(u32x4*)(T1 + row * D + col) = w;
	v_lshlrev_b32_e32 v148, 16, v124
	v_and_b32_e32 v149, 0xffff0000, v124
	v_lshlrev_b32_e32 v150, 16, v168
	v_and_b32_e32 v151, 0xffff0000, v168
	v_pk_fma_f32 v[62:63], v[62:63], v[148:149], v[150:151]
	v_lshlrev_b32_e32 v148, 16, v125
	v_and_b32_e32 v149, 0xffff0000, v125
	v_lshlrev_b32_e32 v150, 16, v169
	v_and_b32_e32 v151, 0xffff0000, v169
	v_pk_fma_f32 v[64:65], v[64:65], v[148:149], v[150:151]
	v_lshlrev_b32_e32 v148, 16, v126
	v_and_b32_e32 v149, 0xffff0000, v126
	v_lshlrev_b32_e32 v150, 16, v170
	v_and_b32_e32 v151, 0xffff0000, v170
	v_pk_fma_f32 v[58:59], v[58:59], v[148:149], v[150:151]
	v_lshlrev_b32_e32 v148, 16, v127
	v_and_b32_e32 v149, 0xffff0000, v127
	v_lshlrev_b32_e32 v150, 16, v171
	v_and_b32_e32 v151, 0xffff0000, v171
	v_pk_fma_f32 v[60:61], v[60:61], v[148:149], v[150:151]
	v_cvt_pk_bf16_f32 v62, v62, v63
	v_cvt_pk_bf16_f32 v63, v64, v65
	v_cvt_pk_bf16_f32 v64, v58, v59
	v_cvt_pk_bf16_f32 v65, v60, v61
	v_add_u32_e32 v159, 0x40000, v157
	global_store_dwordx4 v159, v[62:65], s[6:7]
	s_waitcnt vmcnt(19)
	v_lshlrev_b32_e32 v148, 16, v172
	v_and_b32_e32 v149, 0xffff0000, v172
	v_lshlrev_b32_e32 v150, 16, v116
	v_and_b32_e32 v151, 0xffff0000, v116
	v_pk_fma_f32 v[54:55], v[54:55], v[148:149], v[150:151]
	v_lshlrev_b32_e32 v148, 16, v173
	v_and_b32_e32 v149, 0xffff0000, v173
	v_lshlrev_b32_e32 v150, 16, v117
	v_and_b32_e32 v151, 0xffff0000, v117
	v_pk_fma_f32 v[56:57], v[56:57], v[148:149], v[150:151]
	v_lshlrev_b32_e32 v148, 16, v174
	v_and_b32_e32 v149, 0xffff0000, v174
	v_lshlrev_b32_e32 v150, 16, v118
	v_and_b32_e32 v151, 0xffff0000, v118
	v_pk_fma_f32 v[50:51], v[50:51], v[148:149], v[150:151]
	v_lshlrev_b32_e32 v148, 16, v175
	v_and_b32_e32 v149, 0xffff0000, v175
	v_lshlrev_b32_e32 v150, 16, v119
	v_and_b32_e32 v151, 0xffff0000, v119
	v_pk_fma_f32 v[52:53], v[52:53], v[148:149], v[150:151]
	v_cvt_pk_bf16_f32 v54, v54, v55
	v_cvt_pk_bf16_f32 v55, v56, v57
	v_cvt_pk_bf16_f32 v56, v50, v51
	v_cvt_pk_bf16_f32 v57, v52, v53
	v_add_u32_e32 v159, 0x40000, v157
	global_store_dwordx4 v159, v[54:57], s[6:7] offset:256
	s_waitcnt vmcnt(17)
	v_lshlrev_b32_e32 v148, 16, v176
	v_and_b32_e32 v149, 0xffff0000, v176
	v_lshlrev_b32_e32 v150, 16, v180
	v_and_b32_e32 v151, 0xffff0000, v180
	v_pk_fma_f32 v[46:47], v[46:47], v[148:149], v[150:151]
	v_lshlrev_b32_e32 v148, 16, v177
	v_and_b32_e32 v149, 0xffff0000, v177
	v_lshlrev_b32_e32 v150, 16, v181
	v_and_b32_e32 v151, 0xffff0000, v181
	v_pk_fma_f32 v[48:49], v[48:49], v[148:149], v[150:151]
	v_lshlrev_b32_e32 v148, 16, v178
	v_and_b32_e32 v149, 0xffff0000, v178
	v_lshlrev_b32_e32 v150, 16, v182
	v_and_b32_e32 v151, 0xffff0000, v182
	v_pk_fma_f32 v[42:43], v[42:43], v[148:149], v[150:151]
	v_lshlrev_b32_e32 v148, 16, v179
	v_and_b32_e32 v149, 0xffff0000, v179
	v_lshlrev_b32_e32 v150, 16, v183
	v_and_b32_e32 v151, 0xffff0000, v183
	v_pk_fma_f32 v[44:45], v[44:45], v[148:149], v[150:151]
	v_cvt_pk_bf16_f32 v46, v46, v47
	v_cvt_pk_bf16_f32 v47, v48, v49
	v_cvt_pk_bf16_f32 v48, v42, v43
	v_cvt_pk_bf16_f32 v49, v44, v45
	v_add_u32_e32 v159, 0x48000, v157
	global_store_dwordx4 v159, v[46:49], s[6:7]
	s_waitcnt vmcnt(15)
	v_lshlrev_b32_e32 v148, 16, v108
	v_and_b32_e32 v149, 0xffff0000, v108
	v_lshlrev_b32_e32 v150, 16, v184
	v_and_b32_e32 v151, 0xffff0000, v184
	v_pk_fma_f32 v[38:39], v[38:39], v[148:149], v[150:151]
	v_lshlrev_b32_e32 v148, 16, v109
	v_and_b32_e32 v149, 0xffff0000, v109
	v_lshlrev_b32_e32 v150, 16, v185
	v_and_b32_e32 v151, 0xffff0000, v185
	v_pk_fma_f32 v[40:41], v[40:41], v[148:149], v[150:151]
	v_lshlrev_b32_e32 v148, 16, v110
	v_and_b32_e32 v149, 0xffff0000, v110
	v_lshlrev_b32_e32 v150, 16, v186
	v_and_b32_e32 v151, 0xffff0000, v186
	v_pk_fma_f32 v[34:35], v[34:35], v[148:149], v[150:151]
	v_lshlrev_b32_e32 v148, 16, v111
	v_and_b32_e32 v149, 0xffff0000, v111
	v_lshlrev_b32_e32 v150, 16, v187
	v_and_b32_e32 v151, 0xffff0000, v187
	v_pk_fma_f32 v[36:37], v[36:37], v[148:149], v[150:151]
	v_cvt_pk_bf16_f32 v38, v38, v39
	v_cvt_pk_bf16_f32 v39, v40, v41
	v_cvt_pk_bf16_f32 v40, v34, v35
	v_cvt_pk_bf16_f32 v41, v36, v37
	v_add_u32_e32 v159, 0x48000, v157
	global_store_dwordx4 v159, v[38:41], s[6:7] offset:256
	s_waitcnt vmcnt(14)
; __device__ __forceinline__ unsigned pk2(float lo, float hi) { f32x2 v = {lo, hi}; return __builtin_bit_cast(unsigned, __builtin_convertvector(v, bf2_t)); }
; template <int BIT = 0> __device__ __forceinline__ void st16w(void* p, u32x4 v) { if ((WT_STORES >> BIT) & 1) asm volatile("global_store_dwordx4 %0, %1, off sc1\n\ts_nop 1" :: "v"(p), "v"(v) : "memory"); else *(u32x4*)p = v; }
; __device__ __forceinline__ float bflo(unsigned u) { return __uint_as_float(u << 16); }
; __device__ __forceinline__ float bfhi(unsigned u) { return __uint_as_float(u & 0xffff0000u); }
;     __device__ __forceinline__ void operator()(const f32x4 (&acc)[2][2][4][2], const Unit& u, int wr, int wc, int fr, int fq) const {
;         const int row0 = u.pm * BM + wr * 64 + fr, col0 = u.pn * BM + wc * 32 + 8 * fq;
; #pragma unroll
;         for (int ai = 0; ai < 2; ++ai)
; #pragma unroll
;             for (int m = 0; m < 4; ++m) {
;                 const size_t row = (size_t)(row0 + ai * HALF + m * 16);
; #pragma unroll
;                 for (int bj = 0; bj < 2; ++bj) {
;                     const int col = col0 + bj * HALF;
;                     const u32x4 g = *(const u32x4*)(P + row * INC + goff + col);
;                     const f32x4 a0 = acc[ai][bj][m][0], a1 = acc[ai][bj][m][1];
;                     float o[8] = {bflo(g.x) * a0[0], bfhi(g.x) * a0[1], bflo(g.y) * a0[2], bfhi(g.y) * a0[3], bflo(g.z) * a1[0], bfhi(g.z) * a1[1], bflo(g.w) * a1[2], bfhi(g.w) * a1[3]};
;                     if (mode) { const u32x4 t = *(const u32x4*)(T1 + row * D + col);
;                         o[0] += bflo(t.x); o[1] += bfhi(t.x); o[2] += bflo(t.y); o[3] += bfhi(t.y); o[4] += bflo(t.z); o[5] += bfhi(t.z); o[6] += bflo(t.w); o[7] += bfhi(t.w); }
;                     u32x4 w; w.x = pk2(o[0], o[1]); w.y = pk2(o[2], o[3]); w.z = pk2(o[4], o[5]); w.w = pk2(o[6], o[7]);
;                     if (mode) st16w(MM + row * D + col, w); else *(u32x4*)(T1 + row * D + col) = w;
	v_lshlrev_b32_e32 v148, 16, v188
	v_and_b32_e32 v149, 0xffff0000, v188
	v_lshlrev_b32_e32 v150, 16, v100
	v_and_b32_e32 v151, 0xffff0000, v100
	v_pk_fma_f32 v[30:31], v[30:31], v[148:149], v[150:151]
	v_lshlrev_b32_e32 v148, 16, v189
	v_and_b32_e32 v149, 0xffff0000, v189
	v_lshlrev_b32_e32 v150, 16, v101
	v_and_b32_e32 v151, 0xffff0000, v101
	v_pk_fma_f32 v[32:33], v[32:33], v[148:149], v[150:151]
	v_lshlrev_b32_e32 v148, 16, v190
	v_and_b32_e32 v149, 0xffff0000, v190
	v_lshlrev_b32_e32 v150, 16, v102
	v_and_b32_e32 v151, 0xffff0000, v102
	v_pk_fma_f32 v[26:27], v[26:27], v[148:149], v[150:151]
	v_lshlrev_b32_e32 v148, 16, v191
	v_and_b32_e32 v149, 0xffff0000, v191
	v_lshlrev_b32_e32 v150, 16, v103
	v_and_b32_e32 v151, 0xffff0000, v103
	v_pk_fma_f32 v[28:29], v[28:29], v[148:149], v[150:151]
	v_cvt_pk_bf16_f32 v30, v30, v31
	v_cvt_pk_bf16_f32 v31, v32, v33
	v_cvt_pk_bf16_f32 v32, v26, v27
	v_cvt_pk_bf16_f32 v33, v28, v29
	v_add_u32_e32 v159, 0x50000, v157
	global_store_dwordx4 v159, v[30:33], s[6:7]
	s_waitcnt vmcnt(12)
	v_lshlrev_b32_e32 v148, 16, v192
	v_and_b32_e32 v149, 0xffff0000, v192
	v_lshlrev_b32_e32 v150, 16, v196
	v_and_b32_e32 v151, 0xffff0000, v196
	v_pk_fma_f32 v[22:23], v[22:23], v[148:149], v[150:151]
	v_lshlrev_b32_e32 v148, 16, v193
	v_and_b32_e32 v149, 0xffff0000, v193
	v_lshlrev_b32_e32 v150, 16, v197
	v_and_b32_e32 v151, 0xffff0000, v197
	v_pk_fma_f32 v[24:25], v[24:25], v[148:149], v[150:151]
	v_lshlrev_b32_e32 v148, 16, v194
	v_and_b32_e32 v149, 0xffff0000, v194
	v_lshlrev_b32_e32 v150, 16, v198
	v_and_b32_e32 v151, 0xffff0000, v198
	v_pk_fma_f32 v[18:19], v[18:19], v[148:149], v[150:151]
	v_lshlrev_b32_e32 v148, 16, v195
	v_and_b32_e32 v149, 0xffff0000, v195
	v_lshlrev_b32_e32 v150, 16, v199
	v_and_b32_e32 v151, 0xffff0000, v199
	v_pk_fma_f32 v[20:21], v[20:21], v[148:149], v[150:151]
	v_cvt_pk_bf16_f32 v22, v22, v23
	v_cvt_pk_bf16_f32 v23, v24, v25
	v_cvt_pk_bf16_f32 v24, v18, v19
	v_cvt_pk_bf16_f32 v25, v20, v21
	v_add_u32_e32 v159, 0x50000, v157
	global_store_dwordx4 v159, v[22:25], s[6:7] offset:256
	s_waitcnt vmcnt(10)
	v_lshlrev_b32_e32 v148, 16, v90
	v_and_b32_e32 v149, 0xffff0000, v90
	v_lshlrev_b32_e32 v150, 16, v208
	v_and_b32_e32 v151, 0xffff0000, v208
	v_pk_fma_f32 v[14:15], v[14:15], v[148:149], v[150:151]
	v_lshlrev_b32_e32 v148, 16, v91
	v_and_b32_e32 v149, 0xffff0000, v91
	v_lshlrev_b32_e32 v150, 16, v209
	v_and_b32_e32 v151, 0xffff0000, v209
	v_pk_fma_f32 v[16:17], v[16:17], v[148:149], v[150:151]
	v_lshlrev_b32_e32 v148, 16, v92
	v_and_b32_e32 v149, 0xffff0000, v92
	v_lshlrev_b32_e32 v150, 16, v210
	v_and_b32_e32 v151, 0xffff0000, v210
	v_pk_fma_f32 v[10:11], v[10:11], v[148:149], v[150:151]
	v_lshlrev_b32_e32 v148, 16, v93
	v_and_b32_e32 v149, 0xffff0000, v93
	v_lshlrev_b32_e32 v150, 16, v211
	v_and_b32_e32 v151, 0xffff0000, v211
	v_pk_fma_f32 v[12:13], v[12:13], v[148:149], v[150:151]
	v_cvt_pk_bf16_f32 v14, v14, v15
	v_cvt_pk_bf16_f32 v15, v16, v17
	v_cvt_pk_bf16_f32 v16, v10, v11
	v_cvt_pk_bf16_f32 v17, v12, v13
	v_add_u32_e32 v159, 0x58000, v157
	global_store_dwordx4 v159, v[14:17], s[6:7]
	s_waitcnt vmcnt(9)
	v_lshlrev_b32_e32 v148, 16, v212
	v_and_b32_e32 v149, 0xffff0000, v212
	v_lshlrev_b32_e32 v150, 16, v82
	v_and_b32_e32 v151, 0xffff0000, v82
	v_pk_fma_f32 v[6:7], v[6:7], v[148:149], v[150:151]
	v_lshlrev_b32_e32 v148, 16, v213
	v_and_b32_e32 v149, 0xffff0000, v213
	v_lshlrev_b32_e32 v150, 16, v83
	v_and_b32_e32 v151, 0xffff0000, v83
	v_pk_fma_f32 v[8:9], v[8:9], v[148:149], v[150:151]
	v_lshlrev_b32_e32 v148, 16, v214
	v_and_b32_e32 v149, 0xffff0000, v214
	v_lshlrev_b32_e32 v150, 16, v84
	v_and_b32_e32 v151, 0xffff0000, v84
	v_pk_fma_f32 v[2:3], v[2:3], v[148:149], v[150:151]
	v_lshlrev_b32_e32 v148, 16, v215
	v_and_b32_e32 v149, 0xffff0000, v215
	v_lshlrev_b32_e32 v150, 16, v85
	v_and_b32_e32 v151, 0xffff0000, v85
	v_pk_fma_f32 v[4:5], v[4:5], v[148:149], v[150:151]
	v_cvt_pk_bf16_f32 v6, v6, v7
	v_cvt_pk_bf16_f32 v7, v8, v9
	v_cvt_pk_bf16_f32 v8, v2, v3
	v_cvt_pk_bf16_f32 v9, v4, v5
	v_add_u32_e32 v159, 0x58000, v157
	global_store_dwordx4 v159, v[6:9], s[6:7] offset:256
	s_nop 1
	s_mov_b64 s[22:23], 0x1c00
	s_cbranch_vccnz .LBB13_836
	s_andn2_b64 vcc, exec, s[8:9]
	s_cbranch_vccnz .LBB13_835
	s_barrier
	s_branch .LBB13_835

; template <int NS  > __device__ __forceinline__ f32x4 ctx_tile(Frame& F, const bf16* A, const bf16* Bt, int r0, int c0) {
;     constexpr int K = NS * 256;
;     const int lane = F.lane, w = F.wave, l15 = lane & 15, g = lane >> 4;
;     const bf16* ap = A + (size_t)(r0 + l15) * K + w * (K / 8) + 8 * g;
;     const bf16* bp = Bt + (size_t)(c0 + l15) * K + w * (K / 8) + 8 * g;
;     f32x4 acc[4][2];
; #pragma unroll
;     for (int rt = 0; rt < 4; ++rt) { acc[rt][0] = (f32x4){0.f, 0.f, 0.f, 0.f}; acc[rt][1] = (f32x4){0.f, 0.f, 0.f, 0.f}; }
; #pragma unroll 4
;     for (int s = 0; s < NS; ++s) {
;         bf16x8 af[4], bf[2];
; #pragma unroll
;         for (int rt = 0; rt < 4; ++rt) af[rt] = *(const bf16x8*)(ap + (size_t)(16 * rt) * K + 32 * s);
;         bf[0] = *(const bf16x8*)(bp + 32 * s); bf[1] = *(const bf16x8*)(bp + (size_t)16 * K + 32 * s);
; #pragma unroll
;         for (int rt = 0; rt < 4; ++rt) { acc[rt][0] = __builtin_amdgcn_mfma_f32_16x16x32_bf16(bf[0], af[rt], acc[rt][0], 0, 0, 0); acc[rt][1] = __builtin_amdgcn_mfma_f32_16x16x32_bf16(bf[1], af[rt], acc[rt][1], 0, 0, 0); }
; __global__ void __launch_bounds__(NWAVES * 64, 2) mk_fwd(Args args) {
;     ...
;                 for (int tl = F.vcu; tl < (np - npm) * 128; tl += F.G) {
;                     const int pm = npm + (tl >> 7), r0 = 256 * pm + 64 * ((tl >> 5) & 3), c0 = 32 * (tl & 31);
;                     const int e = __builtin_amdgcn_readfirstlane(((const int*)(ws + WS_PANELE))[pm]);
;                     const f32x4 s = ctx_tile<14>(F, (const bf16*)(ws + WS_HID), (const bf16*)(ws + WS_EXP + (l >> 1) * EXP_STRIDE) + (size_t)NE * 2 * DFE * D + (size_t)e * D * DFE, r0, c0);
.LBB13_1582:
	s_ashr_i32 s4, s29, 7
	s_add_i32 s4, s4, s36
	s_and_b32 s6, s11, 0xc0
	s_and_b32 s15, s13, 0x3e0
	s_lshl_b32 s7, s4, 8
	s_ashr_i32 s5, s4, 31
	v_or_b32_e32 v2, s15, v62
	s_or_b32 s16, s7, s6
	s_lshl_b64 s[4:5], s[4:5], 2
	v_mul_u32_u24_e32 v2, 0xe00, v2
	s_add_u32 s4, s2, s4
	v_lshlrev_b32_e32 v10, 1, v2
	v_or_b32_e32 v2, s16, v62
	s_addc_u32 s5, s3, s5
	v_mad_i64_i32 v[30:31], s[6:7], v2, s86, v[58:59]
	global_load_dword v12, v98, s[4:5]
	s_mov_b32 s4, 0x38000
	v_add_co_u32_e32 v32, vcc, s90, v30
	v_add_co_u32_e64 v50, s[4:5], s4, v30
	s_nop 0
	v_addc_co_u32_e32 v33, vcc, 0, v31, vcc
	v_addc_co_u32_e64 v51, vcc, 0, v31, s[4:5]
	v_mov_b32_e32 v11, v98
	s_mov_b32 s6, 0x54000
	v_mov_b32_e32 v61, v98
	v_add_co_u32_e64 v54, s[6:7], s6, v30
	s_nop 1
	v_addc_co_u32_e64 v55, vcc, 0, v31, s[6:7]
	global_load_dwordx4 v[68:71], v[30:31], off
	global_load_dwordx4 v[72:75], v[32:33], off
	global_load_dwordx4 v[76:79], v[50:51], off
	global_load_dwordx4 v[80:83], v[54:55], off
	global_load_dwordx4 v[84:87], v[30:31], off offset:64
	global_load_dwordx4 v[88:91], v[32:33], off offset:64
	global_load_dwordx4 v[92:95], v[50:51], off offset:64
	global_load_dwordx4 v[100:103], v[54:55], off offset:64
	global_load_dwordx4 v[104:107], v[30:31], off offset:128
	global_load_dwordx4 v[108:111], v[32:33], off offset:128
	global_load_dwordx4 v[112:115], v[50:51], off offset:128
	global_load_dwordx4 v[116:119], v[54:55], off offset:128
	global_load_dwordx4 v[120:123], v[30:31], off offset:192
	global_load_dwordx4 v[124:127], v[32:33], off offset:192
	global_load_dwordx4 v[128:131], v[50:51], off offset:192
	global_load_dwordx4 v[132:135], v[54:55], off offset:192
	global_load_dwordx4 v[136:139], v[30:31], off offset:256
	global_load_dwordx4 v[140:143], v[32:33], off offset:256
	global_load_dwordx4 v[144:147], v[50:51], off offset:256
	global_load_dwordx4 v[148:151], v[54:55], off offset:256
	global_load_dwordx4 v[152:155], v[30:31], off offset:320
	global_load_dwordx4 v[156:159], v[32:33], off offset:320
	global_load_dwordx4 v[160:163], v[50:51], off offset:320
	global_load_dwordx4 v[164:167], v[54:55], off offset:320
	s_waitcnt vmcnt(24)
	v_readfirstlane_b32 s4, v12
	s_mul_hi_i32 s5, s4, 0x700000
	s_mul_i32 s4, s4, 0x700000
	s_add_u32 s4, s34, s4
	s_addc_u32 s5, s35, s5
	v_lshl_add_u64 v[10:11], s[4:5], 0, v[10:11]
	v_lshl_add_u64 v[10:11], s[8:9], 1, v[10:11]
	v_lshl_add_u64 v[52:53], v[10:11], 0, v[60:61]
	v_add_co_u32_e32 v56, vcc, s90, v52
	s_nop 1
	v_addc_co_u32_e32 v57, vcc, 0, v53, vcc
	global_load_dwordx4 v[168:171], v[52:53], off
	global_load_dwordx4 v[172:175], v[56:57], off
	global_load_dwordx4 v[176:179], v[52:53], off offset:64
	global_load_dwordx4 v[180:183], v[56:57], off offset:64
	global_load_dwordx4 v[184:187], v[52:53], off offset:128
	global_load_dwordx4 v[188:191], v[56:57], off offset:128
	global_load_dwordx4 v[192:195], v[52:53], off offset:192
	global_load_dwordx4 v[208:211], v[56:57], off offset:192
	global_load_dwordx4 v[212:215], v[52:53], off offset:256
	global_load_dwordx4 v[216:219], v[56:57], off offset:256
	global_load_dwordx4 v[220:223], v[52:53], off offset:320
	global_load_dwordx4 v[224:227], v[56:57], off offset:320
	s_waitcnt vmcnt(10)
	v_mfma_f32_16x16x32_bf16 v[4:7], v[168:171], v[68:71], 0
	v_mfma_f32_16x16x32_bf16 v[8:11], v[172:175], v[68:71], 0
	v_mfma_f32_16x16x32_bf16 v[12:15], v[168:171], v[72:75], 0
	v_mfma_f32_16x16x32_bf16 v[16:19], v[172:175], v[72:75], 0
	v_mfma_f32_16x16x32_bf16 v[20:23], v[168:171], v[76:79], 0
	v_mfma_f32_16x16x32_bf16 v[24:27], v[172:175], v[76:79], 0
	v_mfma_f32_16x16x32_bf16 v[44:47], v[168:171], v[80:83], 0
	v_mfma_f32_16x16x32_bf16 v[244:247], v[172:175], v[80:83], 0
	global_load_dwordx4 v[228:231], v[30:31], off offset:384
	global_load_dwordx4 v[68:71], v[32:33], off offset:384
	global_load_dwordx4 v[72:75], v[50:51], off offset:384
	global_load_dwordx4 v[76:79], v[54:55], off offset:384
	global_load_dwordx4 v[80:83], v[52:53], off offset:384
	global_load_dwordx4 v[168:171], v[56:57], off offset:384
	s_waitcnt vmcnt(14)
	v_mfma_f32_16x16x32_bf16 v[4:7], v[176:179], v[84:87], v[4:7]
	v_mfma_f32_16x16x32_bf16 v[8:11], v[180:183], v[84:87], v[8:11]
	v_mfma_f32_16x16x32_bf16 v[12:15], v[176:179], v[88:91], v[12:15]
	v_mfma_f32_16x16x32_bf16 v[16:19], v[180:183], v[88:91], v[16:19]
	v_mfma_f32_16x16x32_bf16 v[20:23], v[176:179], v[92:95], v[20:23]
	v_mfma_f32_16x16x32_bf16 v[24:27], v[180:183], v[92:95], v[24:27]
	v_mfma_f32_16x16x32_bf16 v[44:47], v[176:179], v[100:103], v[44:47]
	v_mfma_f32_16x16x32_bf16 v[244:247], v[180:183], v[100:103], v[244:247]
	global_load_dwordx4 v[172:175], v[30:31], off offset:448
	global_load_dwordx4 v[84:87], v[32:33], off offset:448
	global_load_dwordx4 v[88:91], v[50:51], off offset:448
	global_load_dwordx4 v[92:95], v[54:55], off offset:448
	global_load_dwordx4 v[100:103], v[52:53], off offset:448
	global_load_dwordx4 v[176:179], v[56:57], off offset:448
	s_waitcnt vmcnt(18)
	v_mfma_f32_16x16x32_bf16 v[4:7], v[184:187], v[104:107], v[4:7]
	v_mfma_f32_16x16x32_bf16 v[8:11], v[188:191], v[104:107], v[8:11]
	v_mfma_f32_16x16x32_bf16 v[12:15], v[184:187], v[108:111], v[12:15]
	v_mfma_f32_16x16x32_bf16 v[16:19], v[188:191], v[108:111], v[16:19]
	v_mfma_f32_16x16x32_bf16 v[20:23], v[184:187], v[112:115], v[20:23]
	v_mfma_f32_16x16x32_bf16 v[24:27], v[188:191], v[112:115], v[24:27]
	v_mfma_f32_16x16x32_bf16 v[44:47], v[184:187], v[116:119], v[44:47]
	v_mfma_f32_16x16x32_bf16 v[244:247], v[188:191], v[116:119], v[244:247]
	global_load_dwordx4 v[180:183], v[30:31], off offset:512
	global_load_dwordx4 v[104:107], v[32:33], off offset:512
	global_load_dwordx4 v[108:111], v[50:51], off offset:512
	global_load_dwordx4 v[112:115], v[54:55], off offset:512
	global_load_dwordx4 v[116:119], v[52:53], off offset:512
	global_load_dwordx4 v[184:187], v[56:57], off offset:512
	s_waitcnt vmcnt(22)
; template <int NS  > __device__ __forceinline__ f32x4 ctx_tile(Frame& F, const bf16* A, const bf16* Bt, int r0, int c0) {
;     ...
; #pragma unroll 4
;     for (int s = 0; s < NS; ++s) {
;         bf16x8 af[4], bf[2];
; #pragma unroll
;         for (int rt = 0; rt < 4; ++rt) af[rt] = *(const bf16x8*)(ap + (size_t)(16 * rt) * K + 32 * s);
;         bf[0] = *(const bf16x8*)(bp + 32 * s); bf[1] = *(const bf16x8*)(bp + (size_t)16 * K + 32 * s);
; #pragma unroll
;         for (int rt = 0; rt < 4; ++rt) { acc[rt][0] = __builtin_amdgcn_mfma_f32_16x16x32_bf16(bf[0], af[rt], acc[rt][0], 0, 0, 0); acc[rt][1] = __builtin_amdgcn_mfma_f32_16x16x32_bf16(bf[1], af[rt], acc[rt][1], 0, 0, 0); }
;     }
	v_mfma_f32_16x16x32_bf16 v[4:7], v[192:195], v[120:123], v[4:7]
	v_mfma_f32_16x16x32_bf16 v[8:11], v[208:211], v[120:123], v[8:11]
	v_mfma_f32_16x16x32_bf16 v[12:15], v[192:195], v[124:127], v[12:15]
	v_mfma_f32_16x16x32_bf16 v[16:19], v[208:211], v[124:127], v[16:19]
	v_mfma_f32_16x16x32_bf16 v[20:23], v[192:195], v[128:131], v[20:23]
	v_mfma_f32_16x16x32_bf16 v[24:27], v[208:211], v[128:131], v[24:27]
	v_mfma_f32_16x16x32_bf16 v[44:47], v[192:195], v[132:135], v[44:47]
	v_mfma_f32_16x16x32_bf16 v[244:247], v[208:211], v[132:135], v[244:247]
	global_load_dwordx4 v[188:191], v[30:31], off offset:576
	global_load_dwordx4 v[120:123], v[32:33], off offset:576
	global_load_dwordx4 v[124:127], v[50:51], off offset:576
	global_load_dwordx4 v[128:131], v[54:55], off offset:576
	global_load_dwordx4 v[132:135], v[52:53], off offset:576
	global_load_dwordx4 v[192:195], v[56:57], off offset:576
	s_waitcnt vmcnt(26)
	v_mfma_f32_16x16x32_bf16 v[4:7], v[212:215], v[136:139], v[4:7]
	v_mfma_f32_16x16x32_bf16 v[8:11], v[216:219], v[136:139], v[8:11]
	v_mfma_f32_16x16x32_bf16 v[12:15], v[212:215], v[140:143], v[12:15]
	v_mfma_f32_16x16x32_bf16 v[16:19], v[216:219], v[140:143], v[16:19]
	v_mfma_f32_16x16x32_bf16 v[20:23], v[212:215], v[144:147], v[20:23]
	v_mfma_f32_16x16x32_bf16 v[24:27], v[216:219], v[144:147], v[24:27]
	v_mfma_f32_16x16x32_bf16 v[44:47], v[212:215], v[148:151], v[44:47]
	v_mfma_f32_16x16x32_bf16 v[244:247], v[216:219], v[148:151], v[244:247]
	global_load_dwordx4 v[208:211], v[30:31], off offset:640
	global_load_dwordx4 v[136:139], v[32:33], off offset:640
	global_load_dwordx4 v[140:143], v[50:51], off offset:640
	global_load_dwordx4 v[144:147], v[54:55], off offset:640
	global_load_dwordx4 v[148:151], v[52:53], off offset:640
	global_load_dwordx4 v[212:215], v[56:57], off offset:640
	s_waitcnt vmcnt(30)
	v_mfma_f32_16x16x32_bf16 v[4:7], v[220:223], v[152:155], v[4:7]
	v_mfma_f32_16x16x32_bf16 v[8:11], v[224:227], v[152:155], v[8:11]
	v_mfma_f32_16x16x32_bf16 v[12:15], v[220:223], v[156:159], v[12:15]
	v_mfma_f32_16x16x32_bf16 v[16:19], v[224:227], v[156:159], v[16:19]
	v_mfma_f32_16x16x32_bf16 v[20:23], v[220:223], v[160:163], v[20:23]
	v_mfma_f32_16x16x32_bf16 v[24:27], v[224:227], v[160:163], v[24:27]
	v_mfma_f32_16x16x32_bf16 v[44:47], v[220:223], v[164:167], v[44:47]
	v_mfma_f32_16x16x32_bf16 v[244:247], v[224:227], v[164:167], v[244:247]
	global_load_dwordx4 v[216:219], v[30:31], off offset:704
	global_load_dwordx4 v[152:155], v[32:33], off offset:704
	global_load_dwordx4 v[156:159], v[50:51], off offset:704
	global_load_dwordx4 v[160:163], v[54:55], off offset:704
	global_load_dwordx4 v[164:167], v[52:53], off offset:704
	global_load_dwordx4 v[220:223], v[56:57], off offset:704
	s_waitcnt vmcnt(30)
	v_mfma_f32_16x16x32_bf16 v[4:7], v[80:83], v[228:231], v[4:7]
	v_mfma_f32_16x16x32_bf16 v[8:11], v[168:171], v[228:231], v[8:11]
	v_mfma_f32_16x16x32_bf16 v[12:15], v[80:83], v[68:71], v[12:15]
	v_mfma_f32_16x16x32_bf16 v[16:19], v[168:171], v[68:71], v[16:19]
	v_mfma_f32_16x16x32_bf16 v[20:23], v[80:83], v[72:75], v[20:23]
	v_mfma_f32_16x16x32_bf16 v[24:27], v[168:171], v[72:75], v[24:27]
	v_mfma_f32_16x16x32_bf16 v[44:47], v[80:83], v[76:79], v[44:47]
	v_mfma_f32_16x16x32_bf16 v[244:247], v[168:171], v[76:79], v[244:247]
	global_load_dwordx4 v[224:227], v[30:31], off offset:768
	global_load_dwordx4 v[228:231], v[32:33], off offset:768
	global_load_dwordx4 v[68:71], v[50:51], off offset:768
	global_load_dwordx4 v[72:75], v[54:55], off offset:768
	global_load_dwordx4 v[76:79], v[52:53], off offset:768
	global_load_dwordx4 v[80:83], v[56:57], off offset:768
	s_waitcnt vmcnt(30)
	v_mfma_f32_16x16x32_bf16 v[4:7], v[100:103], v[172:175], v[4:7]
	v_mfma_f32_16x16x32_bf16 v[8:11], v[176:179], v[172:175], v[8:11]
	v_mfma_f32_16x16x32_bf16 v[12:15], v[100:103], v[84:87], v[12:15]
	v_mfma_f32_16x16x32_bf16 v[16:19], v[176:179], v[84:87], v[16:19]
	v_mfma_f32_16x16x32_bf16 v[20:23], v[100:103], v[88:91], v[20:23]
	v_mfma_f32_16x16x32_bf16 v[24:27], v[176:179], v[88:91], v[24:27]
	v_mfma_f32_16x16x32_bf16 v[44:47], v[100:103], v[92:95], v[44:47]
	v_mfma_f32_16x16x32_bf16 v[244:247], v[176:179], v[92:95], v[244:247]
	global_load_dwordx4 v[168:171], v[30:31], off offset:832
	global_load_dwordx4 v[172:175], v[32:33], off offset:832
	global_load_dwordx4 v[84:87], v[50:51], off offset:832
	global_load_dwordx4 v[88:91], v[54:55], off offset:832
	global_load_dwordx4 v[92:95], v[52:53], off offset:832
	global_load_dwordx4 v[100:103], v[56:57], off offset:832
	s_waitcnt vmcnt(30)
	v_mfma_f32_16x16x32_bf16 v[4:7], v[116:119], v[180:183], v[4:7]
	v_mfma_f32_16x16x32_bf16 v[8:11], v[184:187], v[180:183], v[8:11]
	v_mfma_f32_16x16x32_bf16 v[12:15], v[116:119], v[104:107], v[12:15]
	v_mfma_f32_16x16x32_bf16 v[16:19], v[184:187], v[104:107], v[16:19]
	v_mfma_f32_16x16x32_bf16 v[20:23], v[116:119], v[108:111], v[20:23]
	v_mfma_f32_16x16x32_bf16 v[24:27], v[184:187], v[108:111], v[24:27]
	v_mfma_f32_16x16x32_bf16 v[44:47], v[116:119], v[112:115], v[44:47]
	v_mfma_f32_16x16x32_bf16 v[244:247], v[184:187], v[112:115], v[244:247]
	s_waitcnt vmcnt(24)
; #define LAS __attribute__((address_space(3)))
; __device__ __forceinline__ unsigned pk2(float lo, float hi) { f32x2 v = {lo, hi}; return __builtin_bit_cast(unsigned, __builtin_convertvector(v, bf2_t)); }
; template <int NS  > __device__ __forceinline__ f32x4 ctx_tile(Frame& F, const bf16* A, const bf16* Bt, int r0, int c0) {
;     ...
; #pragma unroll 4
;     for (int s = 0; s < NS; ++s) {
;         bf16x8 af[4], bf[2];
; #pragma unroll
;         for (int rt = 0; rt < 4; ++rt) af[rt] = *(const bf16x8*)(ap + (size_t)(16 * rt) * K + 32 * s);
;         bf[0] = *(const bf16x8*)(bp + 32 * s); bf[1] = *(const bf16x8*)(bp + (size_t)16 * K + 32 * s);
; #pragma unroll
;         for (int rt = 0; rt < 4; ++rt) { acc[rt][0] = __builtin_amdgcn_mfma_f32_16x16x32_bf16(bf[0], af[rt], acc[rt][0], 0, 0, 0); acc[rt][1] = __builtin_amdgcn_mfma_f32_16x16x32_bf16(bf[1], af[rt], acc[rt][1], 0, 0, 0); }
;     }
;     LAS f32x4* red = (LAS f32x4*)F.lds;
;     __syncthreads();
; #pragma unroll
;     for (int rt = 0; rt < 4; ++rt) { red[(w * 8 + 2 * rt) * 64 + lane] = acc[rt][0]; red[(w * 8 + 2 * rt + 1) * 64 + lane] = acc[rt][1]; }
;     __syncthreads();
;     const int tt = F.tid >> 6;
;     f32x4 v = red[tt * 64 + lane];
; #pragma unroll
;     for (int ww = 1; ww < 8; ++ww) v = v + red[(ww * 8 + tt) * 64 + lane];
;     return v;
; }
; __global__ void __launch_bounds__(NWAVES * 64, 2) mk_fwd(Args args) {
;     ...
;                     const int tt = F.tid >> 6; const size_t row = (size_t)(r0 + 16 * (tt >> 1) + (F.lane & 15)); const int col = c0 + 16 * (tt & 1) + 4 * (F.lane >> 4);
;                     u32x2 o2; o2.x = pk2(s[0], s[1]); o2.y = pk2(s[2], s[3]);
;                     *(u32x2*)((bf16*)(ws + WS_FS) + row * D + col) = o2;
	v_mfma_f32_16x16x32_bf16 v[4:7], v[132:135], v[188:191], v[4:7]
	v_mfma_f32_16x16x32_bf16 v[8:11], v[192:195], v[188:191], v[8:11]
	v_mfma_f32_16x16x32_bf16 v[12:15], v[132:135], v[120:123], v[12:15]
	v_mfma_f32_16x16x32_bf16 v[16:19], v[192:195], v[120:123], v[16:19]
	v_mfma_f32_16x16x32_bf16 v[20:23], v[132:135], v[124:127], v[20:23]
	v_mfma_f32_16x16x32_bf16 v[24:27], v[192:195], v[124:127], v[24:27]
	v_mfma_f32_16x16x32_bf16 v[44:47], v[132:135], v[128:131], v[44:47]
	v_mfma_f32_16x16x32_bf16 v[244:247], v[192:195], v[128:131], v[244:247]
	s_waitcnt vmcnt(18)
	v_mfma_f32_16x16x32_bf16 v[4:7], v[148:151], v[208:211], v[4:7]
	v_mfma_f32_16x16x32_bf16 v[8:11], v[212:215], v[208:211], v[8:11]
	v_mfma_f32_16x16x32_bf16 v[12:15], v[148:151], v[136:139], v[12:15]
	v_mfma_f32_16x16x32_bf16 v[16:19], v[212:215], v[136:139], v[16:19]
	v_mfma_f32_16x16x32_bf16 v[20:23], v[148:151], v[140:143], v[20:23]
	v_mfma_f32_16x16x32_bf16 v[24:27], v[212:215], v[140:143], v[24:27]
	v_mfma_f32_16x16x32_bf16 v[44:47], v[148:151], v[144:147], v[44:47]
	v_mfma_f32_16x16x32_bf16 v[244:247], v[212:215], v[144:147], v[244:247]
	s_waitcnt vmcnt(12)
	v_mfma_f32_16x16x32_bf16 v[4:7], v[164:167], v[216:219], v[4:7]
	v_mfma_f32_16x16x32_bf16 v[8:11], v[220:223], v[216:219], v[8:11]
	v_mfma_f32_16x16x32_bf16 v[12:15], v[164:167], v[152:155], v[12:15]
	v_mfma_f32_16x16x32_bf16 v[16:19], v[220:223], v[152:155], v[16:19]
	v_mfma_f32_16x16x32_bf16 v[20:23], v[164:167], v[156:159], v[20:23]
	v_mfma_f32_16x16x32_bf16 v[24:27], v[220:223], v[156:159], v[24:27]
	v_mfma_f32_16x16x32_bf16 v[44:47], v[164:167], v[160:163], v[44:47]
	v_mfma_f32_16x16x32_bf16 v[244:247], v[220:223], v[160:163], v[244:247]
	s_waitcnt vmcnt(6)
	v_mfma_f32_16x16x32_bf16 v[4:7], v[76:79], v[224:227], v[4:7]
	v_mfma_f32_16x16x32_bf16 v[8:11], v[80:83], v[224:227], v[8:11]
	v_mfma_f32_16x16x32_bf16 v[12:15], v[76:79], v[228:231], v[12:15]
	v_mfma_f32_16x16x32_bf16 v[16:19], v[80:83], v[228:231], v[16:19]
	v_mfma_f32_16x16x32_bf16 v[20:23], v[76:79], v[68:71], v[20:23]
	v_mfma_f32_16x16x32_bf16 v[24:27], v[80:83], v[68:71], v[24:27]
	v_mfma_f32_16x16x32_bf16 v[44:47], v[76:79], v[72:75], v[44:47]
	v_mfma_f32_16x16x32_bf16 v[244:247], v[80:83], v[72:75], v[244:247]
	s_waitcnt vmcnt(0)
	v_mfma_f32_16x16x32_bf16 v[4:7], v[92:95], v[168:171], v[4:7]
	v_mfma_f32_16x16x32_bf16 v[8:11], v[100:103], v[168:171], v[8:11]
	v_mfma_f32_16x16x32_bf16 v[12:15], v[92:95], v[172:175], v[12:15]
	v_mfma_f32_16x16x32_bf16 v[16:19], v[100:103], v[172:175], v[16:19]
	v_mfma_f32_16x16x32_bf16 v[20:23], v[92:95], v[84:87], v[20:23]
	v_mfma_f32_16x16x32_bf16 v[24:27], v[100:103], v[84:87], v[24:27]
	v_mfma_f32_16x16x32_bf16 v[44:47], v[92:95], v[88:91], v[44:47]
	v_mfma_f32_16x16x32_bf16 v[244:247], v[100:103], v[88:91], v[244:247]
	v_or_b32_e32 v61, s15, v1
	s_add_i32 s29, s29, s28
	s_add_i32 s11, s11, s12
	s_add_i32 s13, s13, s14
	s_cmp_ge_i32 s29, s10
	v_mov_b32_e32 v67, v98
	s_barrier
	v_lshlrev_b32_e32 v66, 1, v61
	v_add_u32_e32 v42, s16, v65
	v_ashrrev_i32_e32 v43, 31, v42
	v_lshlrev_b64 v[42:43], 11, v[42:43]
	v_lshl_add_u64 v[38:39], s[0:1], 0, v[42:43]
	v_lshl_add_u64 v[38:39], v[38:39], 0, v[66:67]
	s_nop 7
	ds_write_b128 v63, v[4:7]
	ds_write_b128 v63, v[8:11] offset:1024
	ds_write_b128 v63, v[12:15] offset:2048
	ds_write_b128 v63, v[16:19] offset:3072
	ds_write_b128 v63, v[20:23] offset:4096
	ds_write_b128 v63, v[24:27] offset:5120
	ds_write_b128 v63, v[44:47] offset:6144
	ds_write_b128 v63, v[244:247] offset:7168
	s_waitcnt lgkmcnt(0)
	s_barrier
	ds_read_b128 v[2:5], v64
	ds_read_b128 v[6:9], v64 offset:8192
	ds_read_b128 v[10:13], v64 offset:16384
	ds_read_b128 v[14:17], v64 offset:24576
	ds_read_b128 v[18:21], v64 offset:32768
	ds_read_b128 v[22:25], v64 offset:40960
	ds_read_b128 v[26:29], v64 offset:49152
	ds_read_b128 v[30:33], v64 offset:57344
	s_waitcnt lgkmcnt(6)
	v_pk_add_f32 v[4:5], v[4:5], v[8:9]
	v_pk_add_f32 v[2:3], v[2:3], v[6:7]
	s_waitcnt lgkmcnt(5)
	v_pk_add_f32 v[4:5], v[4:5], v[12:13]
	v_pk_add_f32 v[2:3], v[2:3], v[10:11]
	s_waitcnt lgkmcnt(4)
	v_pk_add_f32 v[4:5], v[4:5], v[16:17]
	v_pk_add_f32 v[2:3], v[2:3], v[14:15]
	s_waitcnt lgkmcnt(3)
	v_pk_add_f32 v[4:5], v[4:5], v[20:21]
	v_pk_add_f32 v[2:3], v[2:3], v[18:19]
	s_waitcnt lgkmcnt(2)
	v_pk_add_f32 v[4:5], v[4:5], v[24:25]
	v_pk_add_f32 v[2:3], v[2:3], v[22:23]
	s_waitcnt lgkmcnt(1)
	v_pk_add_f32 v[4:5], v[4:5], v[28:29]
	v_pk_add_f32 v[2:3], v[2:3], v[26:27]
	s_waitcnt lgkmcnt(0)
	v_pk_add_f32 v[4:5], v[4:5], v[32:33]
	v_pk_add_f32 v[2:3], v[2:3], v[30:31]
	s_nop 0
	v_cvt_pk_bf16_f32 v2, v2, v3
	v_cvt_pk_bf16_f32 v3, v4, v5
	global_store_dwordx2 v[38:39], v[2:3], off
	s_cbranch_scc0 .LBB13_1582
